# MoE k-loop: two B register staging sets, B tile t+3 requested at iteration t (2 k-tiles of B in flight)
# speedup vs baseline: 1.0128x; 1.0128x over previous
.LBB0_1169:
	v_mov_b32_e32 v3, v0
	s_lshl_b32 s4, s87, 8
	v_ashrrev_i32_e32 v1, 6, v3
	v_bfe_u32 v4, v3, 5, 1
	v_readfirstlane_b32 s5, v1
	v_lshlrev_b32_e32 v1, 1, v1
	v_or_b32_e32 v5, v1, v4
	v_bitop3_b32 v1, v1, 3, v4 bitop3:0xc8
	v_lshrrev_b32_e32 v4, 6, v3
	v_bfe_u32 v22, v3, 1, 4
	v_and_b32_e32 v4, 4, v4
	s_lshl_b32 s2, s5, 5
	v_bitop3_b32 v1, v1, v22, v4 bitop3:0x36
	v_lshlrev_b32_e32 v4, 4, v3
	s_and_b32 s2, s2, 0xffffff80
	v_lshlrev_b32_e32 v1, 5, v1
	v_and_b32_e32 v4, 16, v4
	v_lshlrev_b32_e32 v5, 9, v5
	s_add_i32 s8, s4, s2
	v_or3_b32 v1, v1, v5, v4
	s_sub_i32 s8, s86, s8
	s_waitcnt vmcnt(0)
	v_add_u32_e32 v218, 0, v1
	s_add_i32 s8, s8, 15
	v_cvt_pk_bf16_f32 v18, v18, v19
	v_cvt_pk_bf16_f32 v19, v20, v21
	v_cvt_pk_bf16_f32 v20, v14, v15
	v_cvt_pk_bf16_f32 v21, v16, v17
	ds_write_b128 v218, v[18:21] offset:49152
	v_cvt_pk_bf16_f32 v4, v10, v11
	v_cvt_pk_bf16_f32 v5, v12, v13
	v_cvt_pk_bf16_f32 v6, v6, v7
	v_cvt_pk_bf16_f32 v7, v8, v9
	ds_write_b128 v218, v[4:7] offset:57344
	s_ashr_i32 s8, s8, 4
	v_lshl_add_u64 v[4:5], v[202:203], 0, s[66:67]
	global_load_dwordx4 v[224:227], v[4:5], off
	v_med3_i32 v22, s8, 0, 8
	global_load_dwordx4 v[228:231], v[4:5], off offset:16
	s_mov_b64 s[8:9], 0x60000
	v_lshl_add_u64 v[4:5], v[202:203], 0, s[8:9]
	global_load_dwordx4 v[232:235], v[4:5], off
	global_load_dwordx4 v[236:239], v[4:5], off offset:16
	s_mov_b64 s[8:9], 0x80000
	v_lshl_add_u64 v[4:5], v[202:203], 0, s[8:9]
	global_load_dwordx4 v[18:21], v[4:5], off
	global_load_dwordx4 v[14:17], v[4:5], off offset:16
	s_mov_b64 s[8:9], 0xa0000
	v_lshl_add_u64 v[4:5], v[202:203], 0, s[8:9]
	global_load_dwordx4 v[10:13], v[4:5], off
	global_load_dwordx4 v[6:9], v[4:5], off offset:16
	s_waitcnt lgkmcnt(0)
	s_cmp_gt_i32 s35, -1
	s_cselect_b64 s[8:9], -1, 0
	v_readfirstlane_b32 s34, v22
	s_and_b64 s[10:11], s[68:69], s[8:9]
	s_waitcnt lgkmcnt(0)
	s_barrier
	s_and_saveexec_b64 s[8:9], s[10:11]
	s_cbranch_execz .LBB0_1171
	s_lshl_b32 s64, s35, 4
	s_lshl_b64 s[10:11], s[64:65], 2
	s_add_u32 s10, s88, s10
	s_addc_u32 s11, s89, s11
	global_atomic_add v2, v210, s[10:11]

.LBB0_1173:
	v_bfe_u32 v5, v3, 2, 2
	v_and_b32_e32 v22, 12, v3
	v_lshrrev_b32_e32 v4, 4, v3
	v_lshrrev_b32_e64 v22, v22, s90
	v_lshlrev_b32_e32 v23, 8, v3
	v_lshlrev_b32_e32 v24, 9, v5
	s_movk_i32 s8, 0x3000
	v_xor_b32_e32 v4, v22, v4
	v_lshrrev_b32_e32 v22, 2, v3
	v_and_or_b32 v23, v23, s8, v24
	s_lshl_b32 s8, s5, 2
	v_and_b32_e32 v1, 15, v3
	v_and_b32_e32 v22, 4, v22
	s_and_b32 s8, s8, 12
	v_or_b32_e32 v1, s2, v1
	v_lshlrev_b32_e32 v4, 4, v4
	v_bitop3_b32 v5, v22, s8, v5 bitop3:0x36
	v_lshlrev_b32_e32 v3, 3, v3
	v_lshl_or_b32 v5, v5, 5, v23
	v_and_b32_e32 v3, 24, v3
	s_lshl_b32 s33, s5, 10
	v_lshlrev_b32_e32 v1, 6, v1
	v_and_b32_e32 v4, 48, v4
	s_movk_i32 s8, 0x60
	v_or_b32_e32 v214, v5, v3
	s_add_i32 s33, s33, 0
	v_add3_u32 v213, 0, v1, v4
	v_bitop3_b32 v217, v5, 32, v3 bitop3:0x36
	v_bitop3_b32 v216, v5, 64, v3 bitop3:0x36
	v_bitop3_b32 v215, v5, s8, v3 bitop3:0x36
	v_mov_b32_e32 v4, v2
	v_mov_b32_e32 v5, v2
	s_cmp_gt_i32 s34, 0
	s_mov_b64 s[8:9], 0xc0000
	v_mov_b32_e32 v3, v2
	v_mov_b64_e32 v[108:109], v[4:5]
	v_mov_b64_e32 v[116:117], v[4:5]
	v_mov_b64_e32 v[120:121], v[4:5]
	v_mov_b64_e32 v[128:129], v[4:5]
	v_mov_b64_e32 v[124:125], v[4:5]
	v_mov_b64_e32 v[132:133], v[4:5]
	v_mov_b64_e32 v[136:137], v[4:5]
	v_mov_b64_e32 v[140:141], v[4:5]
	v_mov_b64_e32 v[144:145], v[4:5]
	v_mov_b64_e32 v[148:149], v[4:5]
	v_mov_b64_e32 v[112:113], v[4:5]
	v_mov_b64_e32 v[104:105], v[4:5]
	v_mov_b64_e32 v[100:101], v[4:5]
	v_mov_b64_e32 v[92:93], v[4:5]
	v_mov_b64_e32 v[96:97], v[4:5]
	v_mov_b64_e32 v[88:89], v[4:5]
	v_mov_b64_e32 v[84:85], v[4:5]
	v_mov_b64_e32 v[76:77], v[4:5]
	v_mov_b64_e32 v[80:81], v[4:5]
	v_mov_b64_e32 v[72:73], v[4:5]
	v_mov_b64_e32 v[68:69], v[4:5]
	v_mov_b64_e32 v[60:61], v[4:5]
	v_mov_b64_e32 v[64:65], v[4:5]
	v_mov_b64_e32 v[56:57], v[4:5]
	v_mov_b64_e32 v[52:53], v[4:5]
	v_mov_b64_e32 v[44:45], v[4:5]
	v_mov_b64_e32 v[48:49], v[4:5]
	v_mov_b64_e32 v[40:41], v[4:5]
	v_mov_b64_e32 v[36:37], v[4:5]
	v_mov_b64_e32 v[28:29], v[4:5]
	v_mov_b64_e32 v[32:33], v[4:5]
	v_mov_b64_e32 v[24:25], v[4:5]
	s_mov_b32 s2, 2
	s_mov_b32 s5, 0
	s_cselect_b64 s[76:77], -1, 0
	v_lshl_add_u64 v[204:205], v[200:201], 0, s[70:71]
	v_lshl_add_u64 v[206:207], v[198:199], 0, s[70:71]
	v_lshl_add_u64 v[208:209], v[202:203], 0, s[8:9]
	v_mov_b64_e32 v[106:107], v[2:3]
	v_mov_b64_e32 v[114:115], v[2:3]
	v_mov_b64_e32 v[118:119], v[2:3]
	v_mov_b64_e32 v[126:127], v[2:3]
	v_mov_b64_e32 v[122:123], v[2:3]
	v_mov_b64_e32 v[130:131], v[2:3]
	v_mov_b64_e32 v[134:135], v[2:3]
	v_mov_b64_e32 v[138:139], v[2:3]
	v_mov_b64_e32 v[142:143], v[2:3]
	v_mov_b64_e32 v[146:147], v[2:3]
	v_mov_b64_e32 v[110:111], v[2:3]
	v_mov_b64_e32 v[102:103], v[2:3]
	v_mov_b64_e32 v[98:99], v[2:3]
	v_mov_b64_e32 v[90:91], v[2:3]
	v_mov_b64_e32 v[94:95], v[2:3]
	v_mov_b64_e32 v[86:87], v[2:3]
	v_mov_b64_e32 v[82:83], v[2:3]
	v_mov_b64_e32 v[74:75], v[2:3]
	v_mov_b64_e32 v[78:79], v[2:3]
	v_mov_b64_e32 v[70:71], v[2:3]
	v_mov_b64_e32 v[66:67], v[2:3]
	v_mov_b64_e32 v[58:59], v[2:3]
	v_mov_b64_e32 v[62:63], v[2:3]
	v_mov_b64_e32 v[54:55], v[2:3]
	v_mov_b64_e32 v[50:51], v[2:3]
	v_mov_b64_e32 v[42:43], v[2:3]
	v_mov_b64_e32 v[46:47], v[2:3]
	v_mov_b64_e32 v[38:39], v[2:3]
	v_mov_b64_e32 v[34:35], v[2:3]
	v_mov_b64_e32 v[26:27], v[2:3]
	v_mov_b64_e32 v[30:31], v[2:3]
	v_mov_b64_e32 v[22:23], v[2:3]
	s_mov_b32 s34, 0
	s_branch .LBB0_1175
.LBB0_1174:
	s_setprio 0
	s_add_i32 s35, s5, 1
	s_cmp_lg_u32 s5, 2
	s_cselect_b32 s5, s35, 0
	s_add_i32 s35, s2, 1
	s_barrier
	s_cmp_lg_u32 s2, 2
	s_cselect_b32 s2, s35, 0
	s_add_i32 s34, s34, 1
	v_lshl_add_u64 v[204:205], v[204:205], 0, 64
	v_lshl_add_u64 v[206:207], v[206:207], 0, 64
	v_lshl_add_u64 v[208:209], v[208:209], 0, s[66:67]
.LBB0_1175:
	s_bitcmp0_b32 s34, 0
	s_cselect_b32 s8, s91, 0x10000
	s_cselect_b32 s9, 0x10000, s91
	s_add_i32 s8, s8, 0
	v_add_u32_e32 v1, s8, v214
	v_add_u32_e32 v3, s8, v217
	s_waitcnt lgkmcnt(14)
	ds_read_b64_tr_b16 v[150:151], v1
	ds_read_b64_tr_b16 v[152:153], v1 offset:2048
	ds_read_b64_tr_b16 v[154:155], v3
	ds_read_b64_tr_b16 v[156:157], v3 offset:2048
	v_add_u32_e32 v1, s8, v216
	v_add_u32_e32 v3, s8, v215
	s_waitcnt lgkmcnt(14)
	ds_read_b64_tr_b16 v[158:159], v1
	ds_read_b64_tr_b16 v[160:161], v1 offset:2048
	ds_read_b64_tr_b16 v[162:163], v3
	ds_read_b64_tr_b16 v[164:165], v3 offset:2048
	v_lshl_add_u32 v1, s5, 14, v213
	s_waitcnt lgkmcnt(14)
	ds_read_b128 v[194:197], v1
	ds_read_b128 v[190:193], v1 offset:1024
	ds_read_b128 v[186:189], v1 offset:2048
	ds_read_b128 v[182:185], v1 offset:3072
	s_waitcnt lgkmcnt(14)
	ds_read_b128 v[178:181], v1 offset:4096
	ds_read_b128 v[174:177], v1 offset:5120
	ds_read_b128 v[170:173], v1 offset:6144
	ds_read_b128 v[166:169], v1 offset:7168
	s_lshl_b32 s8, s2, 14
	s_add_i32 s8, s33, s8
	s_mov_b32 s35, m0
	s_mov_b32 m0, s8
	s_nop 0
	global_load_lds_dwordx4 v[206:207], off
	s_mov_b32 m0, s35
	s_addk_i32 s8, 0x2000
	s_mov_b32 s35, m0
	s_mov_b32 m0, s8
	s_nop 0
	global_load_lds_dwordx4 v[204:205], off
	s_mov_b32 m0, s35
	v_add_u32_e32 v1, s9, v218
	s_waitcnt vmcnt(6)
	s_nop 0
	v_cvt_pk_bf16_f32 v224, v224, v225
	v_cvt_pk_bf16_f32 v225, v226, v227
	v_cvt_pk_bf16_f32 v226, v228, v229
	v_cvt_pk_bf16_f32 v227, v230, v231
	ds_write_b128 v1, v[224:227]
	v_cvt_pk_bf16_f32 v232, v232, v233
	v_cvt_pk_bf16_f32 v233, v234, v235
	v_cvt_pk_bf16_f32 v234, v236, v237
	v_cvt_pk_bf16_f32 v235, v238, v239
	ds_write_b128 v1, v[232:235] offset:8192
	global_load_dwordx4 v[224:227], v[208:209], off
	global_load_dwordx4 v[228:231], v[208:209], off offset:16
	v_lshl_add_u64 v[4:5], v[208:209], 0, s[62:63]
	global_load_dwordx4 v[232:235], v[4:5], off
	global_load_dwordx4 v[236:239], v[4:5], off offset:16
	s_waitcnt lgkmcnt(0)
	s_barrier
	s_setprio 1
	v_cndmask_b32_e64 v1, 0, 1, s[76:77]
	v_cmp_ne_u32_e64 s[8:9], 1, v1
	s_andn2_b64 vcc, exec, s[76:77]
	s_cbranch_vccnz .Lmoe_end_even
	s_waitcnt lgkmcnt(9)
	v_mfma_f32_16x16x32_bf16 v[146:149], v[150:153], v[194:197], v[146:149]
	v_mfma_f32_16x16x32_bf16 v[142:145], v[154:157], v[194:197], v[142:145]
	v_mfma_f32_16x16x32_bf16 v[138:141], v[158:161], v[194:197], v[138:141]
	v_mfma_f32_16x16x32_bf16 v[134:137], v[162:165], v[194:197], v[134:137]
	s_waitcnt lgkmcnt(8)
	v_mfma_f32_16x16x32_bf16 v[130:133], v[150:153], v[190:193], v[130:133]
	v_mfma_f32_16x16x32_bf16 v[122:125], v[154:157], v[190:193], v[122:125]
	v_mfma_f32_16x16x32_bf16 v[126:129], v[158:161], v[190:193], v[126:129]
	v_mfma_f32_16x16x32_bf16 v[118:121], v[162:165], v[190:193], v[118:121]
	s_waitcnt lgkmcnt(7)
	v_mfma_f32_16x16x32_bf16 v[114:117], v[150:153], v[186:189], v[114:117]
	v_mfma_f32_16x16x32_bf16 v[106:109], v[154:157], v[186:189], v[106:109]
	v_mfma_f32_16x16x32_bf16 v[110:113], v[158:161], v[186:189], v[110:113]
	v_mfma_f32_16x16x32_bf16 v[102:105], v[162:165], v[186:189], v[102:105]
	s_waitcnt lgkmcnt(6)
	v_mfma_f32_16x16x32_bf16 v[98:101], v[150:153], v[182:185], v[98:101]
	v_mfma_f32_16x16x32_bf16 v[90:93], v[154:157], v[182:185], v[90:93]
	v_mfma_f32_16x16x32_bf16 v[94:97], v[158:161], v[182:185], v[94:97]
	v_mfma_f32_16x16x32_bf16 v[86:89], v[162:165], v[182:185], v[86:89]
	s_waitcnt lgkmcnt(5)
	v_mfma_f32_16x16x32_bf16 v[82:85], v[150:153], v[178:181], v[82:85]
	v_mfma_f32_16x16x32_bf16 v[74:77], v[154:157], v[178:181], v[74:77]
	v_mfma_f32_16x16x32_bf16 v[78:81], v[158:161], v[178:181], v[78:81]
	v_mfma_f32_16x16x32_bf16 v[70:73], v[162:165], v[178:181], v[70:73]
	s_waitcnt lgkmcnt(4)
	v_mfma_f32_16x16x32_bf16 v[66:69], v[150:153], v[174:177], v[66:69]
	v_mfma_f32_16x16x32_bf16 v[58:61], v[154:157], v[174:177], v[58:61]
	v_mfma_f32_16x16x32_bf16 v[62:65], v[158:161], v[174:177], v[62:65]
	v_mfma_f32_16x16x32_bf16 v[54:57], v[162:165], v[174:177], v[54:57]
	s_waitcnt lgkmcnt(3)
	v_mfma_f32_16x16x32_bf16 v[50:53], v[150:153], v[170:173], v[50:53]
	v_mfma_f32_16x16x32_bf16 v[42:45], v[154:157], v[170:173], v[42:45]
	v_mfma_f32_16x16x32_bf16 v[46:49], v[158:161], v[170:173], v[46:49]
	v_mfma_f32_16x16x32_bf16 v[38:41], v[162:165], v[170:173], v[38:41]
	s_waitcnt lgkmcnt(2)
	v_mfma_f32_16x16x32_bf16 v[34:37], v[150:153], v[166:169], v[34:37]
	v_mfma_f32_16x16x32_bf16 v[26:29], v[154:157], v[166:169], v[26:29]
	v_mfma_f32_16x16x32_bf16 v[30:33], v[158:161], v[166:169], v[30:33]
	v_mfma_f32_16x16x32_bf16 v[22:25], v[162:165], v[166:169], v[22:25]
.Lmoe_end_even:
	s_setprio 0
	s_add_i32 s35, s5, 1
	s_cmp_lg_u32 s5, 2
	s_cselect_b32 s5, s35, 0
	s_add_i32 s35, s2, 1
	s_barrier
	s_cmp_lg_u32 s2, 2
	s_cselect_b32 s2, s35, 0
	s_add_i32 s34, s34, 1
	v_lshl_add_u64 v[204:205], v[204:205], 0, 64
	v_lshl_add_u64 v[206:207], v[206:207], 0, 64
	v_lshl_add_u64 v[208:209], v[208:209], 0, s[66:67]
	s_cmp_eq_u32 s34, 61
	s_cbranch_scc1 .Lmoe_t61
	s_bitcmp0_b32 s34, 0
	s_cselect_b32 s8, s91, 0x10000
	s_cselect_b32 s9, 0x10000, s91
	s_add_i32 s8, s8, 0
	v_add_u32_e32 v1, s8, v214
	v_add_u32_e32 v3, s8, v217
	s_waitcnt lgkmcnt(14)
	ds_read_b64_tr_b16 v[150:151], v1
	ds_read_b64_tr_b16 v[152:153], v1 offset:2048
	ds_read_b64_tr_b16 v[154:155], v3
	ds_read_b64_tr_b16 v[156:157], v3 offset:2048
	v_add_u32_e32 v1, s8, v216
	v_add_u32_e32 v3, s8, v215
	s_waitcnt lgkmcnt(14)
	ds_read_b64_tr_b16 v[158:159], v1
	ds_read_b64_tr_b16 v[160:161], v1 offset:2048
	ds_read_b64_tr_b16 v[162:163], v3
	ds_read_b64_tr_b16 v[164:165], v3 offset:2048
	v_lshl_add_u32 v1, s5, 14, v213
	s_waitcnt lgkmcnt(14)
	ds_read_b128 v[194:197], v1
	ds_read_b128 v[190:193], v1 offset:1024
	ds_read_b128 v[186:189], v1 offset:2048
	ds_read_b128 v[182:185], v1 offset:3072
	s_waitcnt lgkmcnt(14)
	ds_read_b128 v[178:181], v1 offset:4096
	ds_read_b128 v[174:177], v1 offset:5120
	ds_read_b128 v[170:173], v1 offset:6144
	ds_read_b128 v[166:169], v1 offset:7168
	s_lshl_b32 s8, s2, 14
	s_add_i32 s8, s33, s8
	s_mov_b32 s35, m0
	s_mov_b32 m0, s8
	s_nop 0
	global_load_lds_dwordx4 v[206:207], off
	s_mov_b32 m0, s35
	s_addk_i32 s8, 0x2000
	s_mov_b32 s35, m0
	s_mov_b32 m0, s8
	s_nop 0
	global_load_lds_dwordx4 v[204:205], off
	s_mov_b32 m0, s35
	v_add_u32_e32 v1, s9, v218
	s_waitcnt vmcnt(6)
	s_nop 0
	v_cvt_pk_bf16_f32 v18, v18, v19
	v_cvt_pk_bf16_f32 v19, v20, v21
	v_cvt_pk_bf16_f32 v20, v14, v15
	v_cvt_pk_bf16_f32 v21, v16, v17
	ds_write_b128 v1, v[18:21]
	v_cvt_pk_bf16_f32 v4, v10, v11
	v_cvt_pk_bf16_f32 v5, v12, v13
	v_cvt_pk_bf16_f32 v6, v6, v7
	v_cvt_pk_bf16_f32 v7, v8, v9
	ds_write_b128 v1, v[4:7] offset:8192
	global_load_dwordx4 v[18:21], v[208:209], off
	global_load_dwordx4 v[14:17], v[208:209], off offset:16
	v_lshl_add_u64 v[4:5], v[208:209], 0, s[62:63]
	global_load_dwordx4 v[10:13], v[4:5], off
	global_load_dwordx4 v[6:9], v[4:5], off offset:16
	s_waitcnt lgkmcnt(0)
	s_barrier
	s_setprio 1
	v_cndmask_b32_e64 v1, 0, 1, s[76:77]
	v_cmp_ne_u32_e64 s[8:9], 1, v1
	s_andn2_b64 vcc, exec, s[76:77]
	s_cbranch_vccnz .LBB0_1174
	s_waitcnt lgkmcnt(9)
	v_mfma_f32_16x16x32_bf16 v[146:149], v[150:153], v[194:197], v[146:149]
	v_mfma_f32_16x16x32_bf16 v[142:145], v[154:157], v[194:197], v[142:145]
	v_mfma_f32_16x16x32_bf16 v[138:141], v[158:161], v[194:197], v[138:141]
	v_mfma_f32_16x16x32_bf16 v[134:137], v[162:165], v[194:197], v[134:137]
	s_waitcnt lgkmcnt(8)
	v_mfma_f32_16x16x32_bf16 v[130:133], v[150:153], v[190:193], v[130:133]
	v_mfma_f32_16x16x32_bf16 v[122:125], v[154:157], v[190:193], v[122:125]
	v_mfma_f32_16x16x32_bf16 v[126:129], v[158:161], v[190:193], v[126:129]
	v_mfma_f32_16x16x32_bf16 v[118:121], v[162:165], v[190:193], v[118:121]
	s_waitcnt lgkmcnt(7)
	v_mfma_f32_16x16x32_bf16 v[114:117], v[150:153], v[186:189], v[114:117]
	v_mfma_f32_16x16x32_bf16 v[106:109], v[154:157], v[186:189], v[106:109]
	v_mfma_f32_16x16x32_bf16 v[110:113], v[158:161], v[186:189], v[110:113]
	v_mfma_f32_16x16x32_bf16 v[102:105], v[162:165], v[186:189], v[102:105]
	s_waitcnt lgkmcnt(6)
	v_mfma_f32_16x16x32_bf16 v[98:101], v[150:153], v[182:185], v[98:101]
	v_mfma_f32_16x16x32_bf16 v[90:93], v[154:157], v[182:185], v[90:93]
	v_mfma_f32_16x16x32_bf16 v[94:97], v[158:161], v[182:185], v[94:97]
	v_mfma_f32_16x16x32_bf16 v[86:89], v[162:165], v[182:185], v[86:89]
	s_waitcnt lgkmcnt(5)
	v_mfma_f32_16x16x32_bf16 v[82:85], v[150:153], v[178:181], v[82:85]
	v_mfma_f32_16x16x32_bf16 v[74:77], v[154:157], v[178:181], v[74:77]
	v_mfma_f32_16x16x32_bf16 v[78:81], v[158:161], v[178:181], v[78:81]
	v_mfma_f32_16x16x32_bf16 v[70:73], v[162:165], v[178:181], v[70:73]
	s_waitcnt lgkmcnt(4)
	v_mfma_f32_16x16x32_bf16 v[66:69], v[150:153], v[174:177], v[66:69]
	v_mfma_f32_16x16x32_bf16 v[58:61], v[154:157], v[174:177], v[58:61]
	v_mfma_f32_16x16x32_bf16 v[62:65], v[158:161], v[174:177], v[62:65]
	v_mfma_f32_16x16x32_bf16 v[54:57], v[162:165], v[174:177], v[54:57]
	s_waitcnt lgkmcnt(3)
	v_mfma_f32_16x16x32_bf16 v[50:53], v[150:153], v[170:173], v[50:53]
	v_mfma_f32_16x16x32_bf16 v[42:45], v[154:157], v[170:173], v[42:45]
	v_mfma_f32_16x16x32_bf16 v[46:49], v[158:161], v[170:173], v[46:49]
	v_mfma_f32_16x16x32_bf16 v[38:41], v[162:165], v[170:173], v[38:41]
	s_waitcnt lgkmcnt(2)
	v_mfma_f32_16x16x32_bf16 v[34:37], v[150:153], v[166:169], v[34:37]
	v_mfma_f32_16x16x32_bf16 v[26:29], v[154:157], v[166:169], v[26:29]
	v_mfma_f32_16x16x32_bf16 v[30:33], v[158:161], v[166:169], v[30:33]
	v_mfma_f32_16x16x32_bf16 v[22:25], v[162:165], v[166:169], v[22:25]
	s_branch .LBB0_1174
.Lmoe_t61:
	s_bitcmp0_b32 s34, 0
	s_cselect_b32 s8, s91, 0x10000
	s_cselect_b32 s9, 0x10000, s91
	s_add_i32 s8, s8, 0
	v_add_u32_e32 v1, s8, v214
	v_add_u32_e32 v3, s8, v217
	s_waitcnt lgkmcnt(14)
	ds_read_b64_tr_b16 v[150:151], v1
	ds_read_b64_tr_b16 v[152:153], v1 offset:2048
	ds_read_b64_tr_b16 v[154:155], v3
	ds_read_b64_tr_b16 v[156:157], v3 offset:2048
	v_add_u32_e32 v1, s8, v216
	v_add_u32_e32 v3, s8, v215
	s_waitcnt lgkmcnt(14)
	ds_read_b64_tr_b16 v[158:159], v1
	ds_read_b64_tr_b16 v[160:161], v1 offset:2048
	ds_read_b64_tr_b16 v[162:163], v3
	ds_read_b64_tr_b16 v[164:165], v3 offset:2048
	v_lshl_add_u32 v1, s5, 14, v213
	s_waitcnt lgkmcnt(14)
	ds_read_b128 v[194:197], v1
	ds_read_b128 v[190:193], v1 offset:1024
	ds_read_b128 v[186:189], v1 offset:2048
	ds_read_b128 v[182:185], v1 offset:3072
	s_waitcnt lgkmcnt(14)
	ds_read_b128 v[178:181], v1 offset:4096
	ds_read_b128 v[174:177], v1 offset:5120
	ds_read_b128 v[170:173], v1 offset:6144
	ds_read_b128 v[166:169], v1 offset:7168
	s_lshl_b32 s8, s2, 14
	s_add_i32 s8, s33, s8
	s_mov_b32 s35, m0
	s_mov_b32 m0, s8
	s_nop 0
	global_load_lds_dwordx4 v[206:207], off
	s_mov_b32 m0, s35
	s_addk_i32 s8, 0x2000
	s_mov_b32 s35, m0
	s_mov_b32 m0, s8
	s_nop 0
	global_load_lds_dwordx4 v[204:205], off
	s_mov_b32 m0, s35
	v_add_u32_e32 v1, s9, v218
	s_waitcnt vmcnt(6)
	s_nop 0
	v_cvt_pk_bf16_f32 v18, v18, v19
	v_cvt_pk_bf16_f32 v19, v20, v21
	v_cvt_pk_bf16_f32 v20, v14, v15
	v_cvt_pk_bf16_f32 v21, v16, v17
	ds_write_b128 v1, v[18:21]
	v_cvt_pk_bf16_f32 v4, v10, v11
	v_cvt_pk_bf16_f32 v5, v12, v13
	v_cvt_pk_bf16_f32 v6, v6, v7
	v_cvt_pk_bf16_f32 v7, v8, v9
	ds_write_b128 v1, v[4:7] offset:8192
	s_waitcnt lgkmcnt(0)
	s_barrier
	s_setprio 1
	v_cndmask_b32_e64 v1, 0, 1, s[76:77]
	v_cmp_ne_u32_e64 s[8:9], 1, v1
	s_andn2_b64 vcc, exec, s[76:77]
	s_cbranch_vccnz .Lmoe_end_t61
	s_waitcnt lgkmcnt(9)
	v_mfma_f32_16x16x32_bf16 v[146:149], v[150:153], v[194:197], v[146:149]
	v_mfma_f32_16x16x32_bf16 v[142:145], v[154:157], v[194:197], v[142:145]
	v_mfma_f32_16x16x32_bf16 v[138:141], v[158:161], v[194:197], v[138:141]
	v_mfma_f32_16x16x32_bf16 v[134:137], v[162:165], v[194:197], v[134:137]
	s_waitcnt lgkmcnt(8)
	v_mfma_f32_16x16x32_bf16 v[130:133], v[150:153], v[190:193], v[130:133]
	v_mfma_f32_16x16x32_bf16 v[122:125], v[154:157], v[190:193], v[122:125]
	v_mfma_f32_16x16x32_bf16 v[126:129], v[158:161], v[190:193], v[126:129]
	v_mfma_f32_16x16x32_bf16 v[118:121], v[162:165], v[190:193], v[118:121]
	s_waitcnt lgkmcnt(7)
	v_mfma_f32_16x16x32_bf16 v[114:117], v[150:153], v[186:189], v[114:117]
	v_mfma_f32_16x16x32_bf16 v[106:109], v[154:157], v[186:189], v[106:109]
	v_mfma_f32_16x16x32_bf16 v[110:113], v[158:161], v[186:189], v[110:113]
	v_mfma_f32_16x16x32_bf16 v[102:105], v[162:165], v[186:189], v[102:105]
	s_waitcnt lgkmcnt(6)
	v_mfma_f32_16x16x32_bf16 v[98:101], v[150:153], v[182:185], v[98:101]
	v_mfma_f32_16x16x32_bf16 v[90:93], v[154:157], v[182:185], v[90:93]
	v_mfma_f32_16x16x32_bf16 v[94:97], v[158:161], v[182:185], v[94:97]
	v_mfma_f32_16x16x32_bf16 v[86:89], v[162:165], v[182:185], v[86:89]
	s_waitcnt lgkmcnt(5)
	v_mfma_f32_16x16x32_bf16 v[82:85], v[150:153], v[178:181], v[82:85]
	v_mfma_f32_16x16x32_bf16 v[74:77], v[154:157], v[178:181], v[74:77]
	v_mfma_f32_16x16x32_bf16 v[78:81], v[158:161], v[178:181], v[78:81]
	v_mfma_f32_16x16x32_bf16 v[70:73], v[162:165], v[178:181], v[70:73]
	s_waitcnt lgkmcnt(4)
	v_mfma_f32_16x16x32_bf16 v[66:69], v[150:153], v[174:177], v[66:69]
	v_mfma_f32_16x16x32_bf16 v[58:61], v[154:157], v[174:177], v[58:61]
	v_mfma_f32_16x16x32_bf16 v[62:65], v[158:161], v[174:177], v[62:65]
	v_mfma_f32_16x16x32_bf16 v[54:57], v[162:165], v[174:177], v[54:57]
	s_waitcnt lgkmcnt(3)
	v_mfma_f32_16x16x32_bf16 v[50:53], v[150:153], v[170:173], v[50:53]
	v_mfma_f32_16x16x32_bf16 v[42:45], v[154:157], v[170:173], v[42:45]
	v_mfma_f32_16x16x32_bf16 v[46:49], v[158:161], v[170:173], v[46:49]
	v_mfma_f32_16x16x32_bf16 v[38:41], v[162:165], v[170:173], v[38:41]
	s_waitcnt lgkmcnt(2)
	v_mfma_f32_16x16x32_bf16 v[34:37], v[150:153], v[166:169], v[34:37]
	v_mfma_f32_16x16x32_bf16 v[26:29], v[154:157], v[166:169], v[26:29]
	v_mfma_f32_16x16x32_bf16 v[30:33], v[158:161], v[166:169], v[30:33]
	v_mfma_f32_16x16x32_bf16 v[22:25], v[162:165], v[166:169], v[22:25]

.LBB0_1177:
	v_add_u32_e32 v1, 0, v214
	v_add_u32_e32 v3, 0, v217
	s_waitcnt lgkmcnt(14)
	ds_read_b64_tr_b16 v[150:151], v1 offset:49152
	ds_read_b64_tr_b16 v[152:153], v1 offset:51200
	ds_read_b64_tr_b16 v[154:155], v3 offset:49152
	ds_read_b64_tr_b16 v[156:157], v3 offset:51200
	v_add_u32_e32 v1, 0, v216
	v_add_u32_e32 v3, 0, v215
	s_waitcnt lgkmcnt(14)
	ds_read_b64_tr_b16 v[158:159], v1 offset:49152
	ds_read_b64_tr_b16 v[160:161], v1 offset:51200
	ds_read_b64_tr_b16 v[162:163], v3 offset:49152
	ds_read_b64_tr_b16 v[164:165], v3 offset:51200
	v_lshl_add_u32 v1, s5, 14, v213
	s_waitcnt lgkmcnt(14)
	ds_read_b128 v[194:197], v1
	ds_read_b128 v[190:193], v1 offset:1024
	ds_read_b128 v[186:189], v1 offset:2048
	ds_read_b128 v[182:185], v1 offset:3072
	s_waitcnt lgkmcnt(14)
	ds_read_b128 v[178:181], v1 offset:4096
	ds_read_b128 v[174:177], v1 offset:5120
	ds_read_b128 v[170:173], v1 offset:6144
	ds_read_b128 v[166:169], v1 offset:7168
	v_add_u32_e32 v1, 0x10000, v218
	s_waitcnt vmcnt(0)
	v_mov_b32_e32 v3, 0
	v_cvt_pk_bf16_f32 v204, v224, v225
	v_cvt_pk_bf16_f32 v205, v226, v227
	v_cvt_pk_bf16_f32 v206, v228, v229
	v_cvt_pk_bf16_f32 v207, v230, v231
	ds_write_b128 v1, v[204:207]
	v_add_u32_e32 v1, 0x12000, v218
	v_cvt_pk_bf16_f32 v204, v232, v233
	v_cvt_pk_bf16_f32 v205, v234, v235
	v_cvt_pk_bf16_f32 v206, v236, v237
	v_cvt_pk_bf16_f32 v207, v238, v239
	ds_write_b128 v1, v[204:207]
	s_and_saveexec_b64 s[34:35], s[6:7]
	s_cbranch_execz .LBB0_1179
	s_lshl_b32 s64, s3, 6
	s_lshl_b64 s[76:77], s[64:65], 2
	s_add_u32 s76, s40, s76
	s_addc_u32 s77, s41, s77
	v_mov_b64_e32 v[4:5], s[76:77]
	global_atomic_add v3, v[4:5], v210, off sc0
